# mLSTM state pass normaliser update: LDS reads issued 1.5 groups ahead of the serial FMA chain (unrolled, two register sets, counted lgkmcnt), same FMA order; on top of packed-SwiGLU stack
# speedup vs baseline: 1.0069x; 1.0069x over previous
; #define LAS __attribute__((address_space(3)))
; template <int DK, int DVB, bool MLSTM>
; __device__ __forceinline__ void state_unit2(LAS unsigned char* lds, LAS unsigned char* ldstab, const StateArgs a, const int wv) {
;     ...
;             if (tid < DK) { float s = 0.f; const int pnl = tid >> 7, col = tid & 127; const LAS unsigned char* kp = lds + half * BUFSZ + pnl * 16384 + (col & 7) * 2;
;                 for (int p = 0; p < 64; ++p) s += bf2f(*(const LAS bf16_t*)(kp + off_a(p, col >> 3))) * wt[64 * half + p];
;                 nacc = (half == 0 ? eF * nacc : nacc) + s; }
.LBB0_567:
	v_mov_b32_e32 v98, s69
	v_add_u32_e32 v98, 0x21500, v98
	v_xor_b32_e32 v96, 0, v51
	v_lshlrev_b32_e32 v96, 4, v96
	v_and_b32_e32 v96, 48, v96
	v_add_u32_e32 v96, v96, v37
	ds_read_b128 v[80:83], v98
	ds_read_u16 v84, v96
	ds_read_u16 v85, v96 offset:64
	ds_read_u16 v86, v96 offset:128
	ds_read_u16 v87, v96 offset:192
	v_xor_b32_e32 v97, 1, v51
	v_lshlrev_b32_e32 v97, 4, v97
	v_and_b32_e32 v97, 48, v97
	v_add_u32_e32 v97, v97, v37
	ds_read_b128 v[88:91], v98 offset:16
	ds_read_u16 v92, v97 offset:256
	ds_read_u16 v93, v97 offset:320
	ds_read_u16 v94, v97 offset:384
	ds_read_u16 v95, v97 offset:448
	v_xor_b32_e32 v116, 2, v51
	v_lshlrev_b32_e32 v116, 4, v116
	v_and_b32_e32 v116, 48, v116
	v_add_u32_e32 v116, v116, v37
	ds_read_b128 v[100:103], v98 offset:32
	ds_read_u16 v104, v116 offset:2048
	ds_read_u16 v105, v116 offset:2112
	ds_read_u16 v106, v116 offset:2176
	ds_read_u16 v107, v116 offset:2240
	s_waitcnt lgkmcnt(5)
	v_lshlrev_b32_e32 v84, 16, v84
	v_fmac_f32_e32 v35, v80, v84
	v_lshlrev_b32_e32 v85, 16, v85
	v_fmac_f32_e32 v35, v81, v85
	v_lshlrev_b32_e32 v86, 16, v86
	v_fmac_f32_e32 v35, v82, v86
	v_lshlrev_b32_e32 v87, 16, v87
	v_fmac_f32_e32 v35, v83, v87
	v_lshlrev_b32_e32 v92, 16, v92
	v_fmac_f32_e32 v35, v88, v92
	v_lshlrev_b32_e32 v93, 16, v93
	v_fmac_f32_e32 v35, v89, v93
	v_lshlrev_b32_e32 v94, 16, v94
	v_fmac_f32_e32 v35, v90, v94
	v_lshlrev_b32_e32 v95, 16, v95
	v_fmac_f32_e32 v35, v91, v95
	v_xor_b32_e32 v117, 3, v51
	v_lshlrev_b32_e32 v117, 4, v117
	v_and_b32_e32 v117, 48, v117
	v_add_u32_e32 v117, v117, v37
	ds_read_b128 v[108:111], v98 offset:48
	ds_read_u16 v112, v117 offset:2304
	ds_read_u16 v113, v117 offset:2368
	ds_read_u16 v114, v117 offset:2432
	ds_read_u16 v115, v117 offset:2496
	v_xor_b32_e32 v96, 4, v51
	v_lshlrev_b32_e32 v96, 4, v96
	v_and_b32_e32 v96, 48, v96
	v_add_u32_e32 v96, v96, v37
	ds_read_b128 v[80:83], v98 offset:64
	ds_read_u16 v84, v96 offset:4096
	ds_read_u16 v85, v96 offset:4160
	ds_read_u16 v86, v96 offset:4224
	ds_read_u16 v87, v96 offset:4288
	s_waitcnt lgkmcnt(5)
	v_lshlrev_b32_e32 v104, 16, v104
	v_fmac_f32_e32 v35, v100, v104
	v_lshlrev_b32_e32 v105, 16, v105
	v_fmac_f32_e32 v35, v101, v105
	v_lshlrev_b32_e32 v106, 16, v106
	v_fmac_f32_e32 v35, v102, v106
	v_lshlrev_b32_e32 v107, 16, v107
	v_fmac_f32_e32 v35, v103, v107
	v_lshlrev_b32_e32 v112, 16, v112
	v_fmac_f32_e32 v35, v108, v112
	v_lshlrev_b32_e32 v113, 16, v113
	v_fmac_f32_e32 v35, v109, v113
	v_lshlrev_b32_e32 v114, 16, v114
	v_fmac_f32_e32 v35, v110, v114
	v_lshlrev_b32_e32 v115, 16, v115
	v_fmac_f32_e32 v35, v111, v115
	v_xor_b32_e32 v97, 5, v51
	v_lshlrev_b32_e32 v97, 4, v97
	v_and_b32_e32 v97, 48, v97
	v_add_u32_e32 v97, v97, v37
	ds_read_b128 v[88:91], v98 offset:80
	ds_read_u16 v92, v97 offset:4352
	ds_read_u16 v93, v97 offset:4416
	ds_read_u16 v94, v97 offset:4480
	ds_read_u16 v95, v97 offset:4544
	v_xor_b32_e32 v116, 6, v51
	v_lshlrev_b32_e32 v116, 4, v116
	v_and_b32_e32 v116, 48, v116
	v_add_u32_e32 v116, v116, v37
	ds_read_b128 v[100:103], v98 offset:96
	ds_read_u16 v104, v116 offset:6144
	ds_read_u16 v105, v116 offset:6208
	ds_read_u16 v106, v116 offset:6272
	ds_read_u16 v107, v116 offset:6336
	s_waitcnt lgkmcnt(5)
	v_lshlrev_b32_e32 v84, 16, v84
	v_fmac_f32_e32 v35, v80, v84
	v_lshlrev_b32_e32 v85, 16, v85
	v_fmac_f32_e32 v35, v81, v85
	v_lshlrev_b32_e32 v86, 16, v86
	v_fmac_f32_e32 v35, v82, v86
	v_lshlrev_b32_e32 v87, 16, v87
	v_fmac_f32_e32 v35, v83, v87
	v_lshlrev_b32_e32 v92, 16, v92
	v_fmac_f32_e32 v35, v88, v92
	v_lshlrev_b32_e32 v93, 16, v93
	v_fmac_f32_e32 v35, v89, v93
	v_lshlrev_b32_e32 v94, 16, v94
	v_fmac_f32_e32 v35, v90, v94
	v_lshlrev_b32_e32 v95, 16, v95
	v_fmac_f32_e32 v35, v91, v95
	v_xor_b32_e32 v117, 7, v51
	v_lshlrev_b32_e32 v117, 4, v117
	v_and_b32_e32 v117, 48, v117
	v_add_u32_e32 v117, v117, v37
	ds_read_b128 v[108:111], v98 offset:112
	ds_read_u16 v112, v117 offset:6400
	ds_read_u16 v113, v117 offset:6464
	ds_read_u16 v114, v117 offset:6528
	ds_read_u16 v115, v117 offset:6592
	v_xor_b32_e32 v96, 8, v51
	v_lshlrev_b32_e32 v96, 4, v96
	v_and_b32_e32 v96, 48, v96
	v_add_u32_e32 v96, v96, v37
	ds_read_b128 v[80:83], v98 offset:128
	ds_read_u16 v84, v96 offset:8192
	ds_read_u16 v85, v96 offset:8256
	ds_read_u16 v86, v96 offset:8320
	ds_read_u16 v87, v96 offset:8384
	s_waitcnt lgkmcnt(5)
; #define LAS __attribute__((address_space(3)))
; template <int DK, int DVB, bool MLSTM>
; __device__ __forceinline__ void state_unit2(LAS unsigned char* lds, LAS unsigned char* ldstab, const StateArgs a, const int wv) {
;     ...
;             if (tid < DK) { float s = 0.f; const int pnl = tid >> 7, col = tid & 127; const LAS unsigned char* kp = lds + half * BUFSZ + pnl * 16384 + (col & 7) * 2;
;                 for (int p = 0; p < 64; ++p) s += bf2f(*(const LAS bf16_t*)(kp + off_a(p, col >> 3))) * wt[64 * half + p];
;                 nacc = (half == 0 ? eF * nacc : nacc) + s; }
	v_lshlrev_b32_e32 v104, 16, v104
	v_fmac_f32_e32 v35, v100, v104
	v_lshlrev_b32_e32 v105, 16, v105
	v_fmac_f32_e32 v35, v101, v105
	v_lshlrev_b32_e32 v106, 16, v106
	v_fmac_f32_e32 v35, v102, v106
	v_lshlrev_b32_e32 v107, 16, v107
	v_fmac_f32_e32 v35, v103, v107
	v_lshlrev_b32_e32 v112, 16, v112
	v_fmac_f32_e32 v35, v108, v112
	v_lshlrev_b32_e32 v113, 16, v113
	v_fmac_f32_e32 v35, v109, v113
	v_lshlrev_b32_e32 v114, 16, v114
	v_fmac_f32_e32 v35, v110, v114
	v_lshlrev_b32_e32 v115, 16, v115
	v_fmac_f32_e32 v35, v111, v115
	v_xor_b32_e32 v97, 9, v51
	v_lshlrev_b32_e32 v97, 4, v97
	v_and_b32_e32 v97, 48, v97
	v_add_u32_e32 v97, v97, v37
	ds_read_b128 v[88:91], v98 offset:144
	ds_read_u16 v92, v97 offset:8448
	ds_read_u16 v93, v97 offset:8512
	ds_read_u16 v94, v97 offset:8576
	ds_read_u16 v95, v97 offset:8640
	v_xor_b32_e32 v116, 10, v51
	v_lshlrev_b32_e32 v116, 4, v116
	v_and_b32_e32 v116, 48, v116
	v_add_u32_e32 v116, v116, v37
	ds_read_b128 v[100:103], v98 offset:160
	ds_read_u16 v104, v116 offset:10240
	ds_read_u16 v105, v116 offset:10304
	ds_read_u16 v106, v116 offset:10368
	ds_read_u16 v107, v116 offset:10432
	s_waitcnt lgkmcnt(5)
	v_lshlrev_b32_e32 v84, 16, v84
	v_fmac_f32_e32 v35, v80, v84
	v_lshlrev_b32_e32 v85, 16, v85
	v_fmac_f32_e32 v35, v81, v85
	v_lshlrev_b32_e32 v86, 16, v86
	v_fmac_f32_e32 v35, v82, v86
	v_lshlrev_b32_e32 v87, 16, v87
	v_fmac_f32_e32 v35, v83, v87
	v_lshlrev_b32_e32 v92, 16, v92
	v_fmac_f32_e32 v35, v88, v92
	v_lshlrev_b32_e32 v93, 16, v93
	v_fmac_f32_e32 v35, v89, v93
	v_lshlrev_b32_e32 v94, 16, v94
	v_fmac_f32_e32 v35, v90, v94
	v_lshlrev_b32_e32 v95, 16, v95
	v_fmac_f32_e32 v35, v91, v95
	v_xor_b32_e32 v117, 11, v51
	v_lshlrev_b32_e32 v117, 4, v117
	v_and_b32_e32 v117, 48, v117
	v_add_u32_e32 v117, v117, v37
	ds_read_b128 v[108:111], v98 offset:176
	ds_read_u16 v112, v117 offset:10496
	ds_read_u16 v113, v117 offset:10560
	ds_read_u16 v114, v117 offset:10624
	ds_read_u16 v115, v117 offset:10688
	v_xor_b32_e32 v96, 12, v51
	v_lshlrev_b32_e32 v96, 4, v96
	v_and_b32_e32 v96, 48, v96
	v_add_u32_e32 v96, v96, v37
	ds_read_b128 v[80:83], v98 offset:192
	ds_read_u16 v84, v96 offset:12288
	ds_read_u16 v85, v96 offset:12352
	ds_read_u16 v86, v96 offset:12416
	ds_read_u16 v87, v96 offset:12480
	s_waitcnt lgkmcnt(5)
	v_lshlrev_b32_e32 v104, 16, v104
	v_fmac_f32_e32 v35, v100, v104
	v_lshlrev_b32_e32 v105, 16, v105
	v_fmac_f32_e32 v35, v101, v105
	v_lshlrev_b32_e32 v106, 16, v106
	v_fmac_f32_e32 v35, v102, v106
	v_lshlrev_b32_e32 v107, 16, v107
	v_fmac_f32_e32 v35, v103, v107
	v_lshlrev_b32_e32 v112, 16, v112
	v_fmac_f32_e32 v35, v108, v112
	v_lshlrev_b32_e32 v113, 16, v113
	v_fmac_f32_e32 v35, v109, v113
	v_lshlrev_b32_e32 v114, 16, v114
	v_fmac_f32_e32 v35, v110, v114
	v_lshlrev_b32_e32 v115, 16, v115
	v_fmac_f32_e32 v35, v111, v115
	v_xor_b32_e32 v97, 13, v51
	v_lshlrev_b32_e32 v97, 4, v97
	v_and_b32_e32 v97, 48, v97
	v_add_u32_e32 v97, v97, v37
	ds_read_b128 v[88:91], v98 offset:208
	ds_read_u16 v92, v97 offset:12544
	ds_read_u16 v93, v97 offset:12608
	ds_read_u16 v94, v97 offset:12672
	ds_read_u16 v95, v97 offset:12736
	v_xor_b32_e32 v116, 14, v51
	v_lshlrev_b32_e32 v116, 4, v116
	v_and_b32_e32 v116, 48, v116
	v_add_u32_e32 v116, v116, v37
	ds_read_b128 v[100:103], v98 offset:224
	ds_read_u16 v104, v116 offset:14336
	ds_read_u16 v105, v116 offset:14400
	ds_read_u16 v106, v116 offset:14464
	ds_read_u16 v107, v116 offset:14528
	s_waitcnt lgkmcnt(5)
	v_lshlrev_b32_e32 v84, 16, v84
	v_fmac_f32_e32 v35, v80, v84
	v_lshlrev_b32_e32 v85, 16, v85
	v_fmac_f32_e32 v35, v81, v85
	v_lshlrev_b32_e32 v86, 16, v86
	v_fmac_f32_e32 v35, v82, v86
	v_lshlrev_b32_e32 v87, 16, v87
	v_fmac_f32_e32 v35, v83, v87
	v_lshlrev_b32_e32 v92, 16, v92
	v_fmac_f32_e32 v35, v88, v92
	v_lshlrev_b32_e32 v93, 16, v93
	v_fmac_f32_e32 v35, v89, v93
	v_lshlrev_b32_e32 v94, 16, v94
	v_fmac_f32_e32 v35, v90, v94
	v_lshlrev_b32_e32 v95, 16, v95
	v_fmac_f32_e32 v35, v91, v95
	v_xor_b32_e32 v117, 15, v51
	v_lshlrev_b32_e32 v117, 4, v117
	v_and_b32_e32 v117, 48, v117
	v_add_u32_e32 v117, v117, v37
	ds_read_b128 v[108:111], v98 offset:240
	ds_read_u16 v112, v117 offset:14592
	ds_read_u16 v113, v117 offset:14656
	ds_read_u16 v114, v117 offset:14720
	ds_read_u16 v115, v117 offset:14784
	s_waitcnt lgkmcnt(0)
	v_lshlrev_b32_e32 v104, 16, v104
	v_fmac_f32_e32 v35, v100, v104
	v_lshlrev_b32_e32 v105, 16, v105
	v_fmac_f32_e32 v35, v101, v105
	v_lshlrev_b32_e32 v106, 16, v106
	v_fmac_f32_e32 v35, v102, v106
	v_lshlrev_b32_e32 v107, 16, v107
	v_fmac_f32_e32 v35, v103, v107
	v_lshlrev_b32_e32 v112, 16, v112
	v_fmac_f32_e32 v35, v108, v112
	v_lshlrev_b32_e32 v113, 16, v113
	v_fmac_f32_e32 v35, v109, v113
	v_lshlrev_b32_e32 v114, 16, v114
	v_fmac_f32_e32 v35, v110, v114
	v_lshlrev_b32_e32 v115, 16, v115
	v_fmac_f32_e32 v35, v111, v115
	v_mul_f32_e32 v37, v60, v44
	v_cndmask_b32_e64 v37, v60, v37, s[6:7]
	v_add_f32_e32 v60, v37, v35
	s_branch .LBB0_554
